# v010 + dense FFN up-projection unit order: row-panel group size 2 -> 4
# speedup vs baseline: 1.0076x; 1.0076x over previous
;     __device__ __forceinline__ size_t boff(const Unit& u) const { return (size_t)__builtin_amdgcn_readfirstlane(panel_e[u.pm]) * estride; }
; #define PG8_SETA(v, u) do { if constexpr (Sched::GATHER) { _Pragma("unroll") for (int h_ = 0; h_ < 2; ++h_) _Pragma("unroll") for (int i_ = 0; i_ < 2; ++i_) { \
;         int R_, C_; stage_rc(tid * 16 + i_ * 8192, R_, C_); int tok_ = S.arow[(u).pm * BM + h_ * HALF + R_]; tok_ = tok_ < 0 ? 0 : tok_; (v)[h_][i_] = (unsigned)(tok_ * K + C_) * 2u; } } } while (0)
; #define PG8_STAGE_A(bufoff, h, ptr, nsel) do { if constexpr (Sched::GATHER) { if (nsel) PG8_STAGE_X(bufoff, ptr, vAn[h], PG8_A_AUX); else PG8_STAGE_X(bufoff, ptr, vAc[h], PG8_A_AUX); } \
;         else PG8_STAGE_X(bufoff, (ptr) + (h) * hstep, voffA, PG8_A_AUX); } while (0)
; #define PG8_STAGE(bufoff, gbase, voff) PG8_STAGE_X(bufoff, gbase, voff, PG8_B_AUX)
; #define PG8_BAR __builtin_amdgcn_s_barrier()
;     __host__ __device__ bool next(int i, Unit& u) const {
;         const long L = (long)i * G + c; if (L >= nwg) return false;
;         int wgid = (int)L; { const int q = nwg / NXCD, r = nwg % NXCD, xcd = wgid % NXCD; int off = wgid / NXCD; if (rev & 2) off = (xcd < r ? q + 1 : q) - 1 - off;
;             wgid = (xcd < r ? xcd * (q + 1) : r * (q + 1) + (xcd - r) * q) + off; }
;         const int nig = wgm * nN, gid = wgid / nig, fm = gid * wgm, gsz = (nM - fm) < wgm ? (nM - fm) : wgm;
;         u.pm = fm + ((wgid % nig) % gsz); u.pn = (wgid % nig) / gsz; if (rev & 1) u.pn = nN - 1 - u.pn; return true;
; template <class Epi, class Sched, bool ALIGN_EPI = false, bool SP2 = false>
; __device__ __forceinline__ void gemm_phase(PG8_LAS unsigned char* lds, const Gemm g, const Sched& S, const Epi& E) {
;     ...
;     const char* cA = Sched::GATHER ? (const char*)g.A : (const char*)g.A + (size_t)cur.pm * tstep; PG8_SETA(vAc, cur); const char* cB = (const char*)g.Bt + S.boff(cur) + (size_t)cur.pn * tstep;
;     S.a_ready(cur);
;     if constexpr (SP2) {
;         PG8_STAGE(PG8_SB(0, 0), cB, voffB); PG8_STAGE(PG8_SB(0, 1), cB + hstep, voffB); PG8_STAGE_A(PG8_SA(0, 0), 0, cA, false); PG8_STAGE_A(PG8_SA(0, 1), 1, cA, false);
;         if (wr == 1) PG8_BAR;
.LBB13_1397:
	v_cndmask_b32_e64 v1, 0, 1, s[38:39]
	s_andn2_b64 vcc, exec, s[4:5]
	v_cmp_ne_u32_e64 s[42:43], 1, v1
	s_cbranch_vccnz .LBB13_1513
	v_readlane_b32 s2, v249, 1
	v_readlane_b32 s3, v249, 2
	s_load_dwordx2 s[2:3], s[2:3], 0xe8
	s_mov_b32 s0, s77
	v_mov_b32_e32 v1, v0
	s_mov_b64 s[8:9], 0
	s_waitcnt lgkmcnt(0)
	s_add_u32 s10, s2, s8
	s_addc_u32 s11, s3, s9
	s_add_i32 s2, s0, 0
	s_add_u32 s14, s10, 0x20700000
	s_addc_u32 s15, s11, 0
	s_lshr_b32 s38, s68, 1
	s_mov_b32 s44, s56
	v_readlane_b32 s45, v249, 0
	s_add_u32 s16, s10, 0x22800000
	s_addc_u32 s17, s11, 0
	s_ashr_i32 s46, s45, 31
	s_lshr_b32 s0, s46, 29
	s_add_i32 s0, s45, s0
	s_ashr_i32 s39, s0, 3
	s_and_b32 s0, s0, -8
	s_sub_i32 s40, s45, s0
	s_add_i32 s47, s2, 0x10000
	s_add_i32 s50, s2, 0x14000
	s_add_i32 s51, s2, 0x18000
	s_add_i32 s56, s2, 0x1c000
	s_ashr_i32 s57, s44, 31
	s_and_b64 vcc, exec, s[42:43]
	s_mov_b64 s[6:7], -1
	s_cbranch_vccnz .LBB13_1420
	v_readlane_b32 s0, v249, 59
	v_readlane_b32 s1, v249, 60
	s_and_b64 s[0:1], s[0:1], exec
	s_cselect_b32 s3, 64, 0x42
	s_mul_i32 s76, s3, 22
	s_waitcnt vmcnt(0)
	v_mov_b32_e32 v8, v0
	s_cmp_ge_i32 s45, s76
	s_nop 0
	v_readfirstlane_b32 s6, v8
	s_cbranch_scc1 .LBB13_1419
	v_lshlrev_b32_e32 v1, 4, v8
	v_add_u32_e32 v3, 0x2000, v1
	v_ashrrev_i32_e32 v2, 31, v3
	v_lshrrev_b32_e32 v2, 22, v2
	v_add_u32_e32 v2, v3, v2
	v_ashrrev_i32_e32 v2, 10, v2
	v_mul_i32_i24_e32 v4, 0x400, v2
	v_sub_u32_e32 v3, v3, v4
	v_lshrrev_b32_e32 v4, 4, v3
	v_bitop3_b32 v4, v4, v3, 32 bitop3:0x6c
	v_ashrrev_i32_e32 v3, 31, v4
	v_lshrrev_b32_e32 v3, 26, v3
	v_add_u32_e32 v5, v4, v3
	v_lshlrev_b32_e32 v6, 3, v2
	v_ashrrev_i32_e32 v3, 6, v5
	v_and_b32_e32 v6, -16, v6
	v_add_u32_e32 v6, v3, v6
	v_and_b32_e32 v7, 3, v3
	s_mov_b32 s4, 0x1fffe0
	v_lshrrev_b32_e32 v9, 2, v6
	v_lshlrev_b32_e32 v10, 1, v6
	v_and_b32_e32 v5, 0xc0, v5
	v_and_or_b32 v7, v6, s4, v7
	v_and_b32_e32 v9, 4, v9
	v_and_b32_e32 v10, 24, v10
	v_sub_u32_e32 v4, v4, v5
	v_or3_b32 v7, v7, v9, v10
	v_lshlrev_b32_e32 v9, 5, v2
	v_ashrrev_i16_sdwa v4, v238, sext(v4) dst_sel:DWORD dst_unused:UNUSED_PAD src0_sel:DWORD src1_sel:BYTE_0
	v_and_b32_e32 v9, 32, v9
	v_bfe_i32 v4, v4, 0, 16
	s_ashr_i32 s12, s6, 6
	v_add_lshl_u32 v5, v9, v4, 1
	s_ashr_i32 s13, s6, 8
	s_lshl_b32 s7, s12, 10
	s_mul_i32 s0, s38, 0x1080000
	v_lshl_add_u32 v132, v7, 11, v5
	v_lshl_add_u32 v134, v6, 11, v5
	v_bfe_i32 v5, v8, 27, 1
	s_add_u32 s0, s10, s0
	v_lshrrev_b32_e32 v5, 22, v5
	s_addc_u32 s1, s11, 0
	v_add_u32_e32 v5, v1, v5
	v_writelane_b32 v249, s42, 55
	s_add_u32 s41, s0, 0x5400000
	v_and_b32_e32 v5, 0xfffffc00, v5
	v_writelane_b32 v249, s43, 56
	s_addc_u32 s42, s1, 0
	s_lshr_b32 s43, s76, 3
	s_and_b32 s48, s76, 4
	v_sub_u32_e32 v1, v1, v5
	s_add_i32 s49, s43, 1
	s_sub_i32 s0, s40, s48
	v_lshrrev_b32_e32 v5, 4, v1
	v_ashrrev_i32_e32 v6, 31, v8
	s_mul_i32 s53, s49, s48
	s_mul_i32 s0, s0, s43
	v_bitop3_b32 v1, v5, v1, 32 bitop3:0x6c
	v_lshrrev_b32_e32 v6, 26, v6
	s_add_i32 s0, s0, s53
	v_ashrrev_i32_e32 v5, 31, v1
	v_add_u32_e32 v6, v8, v6
	s_cmp_lt_i32 s40, s48
	s_mul_i32 s1, s40, s49
	v_lshrrev_b32_e32 v5, 26, v5
	v_ashrrev_i32_e32 v6, 6, v6
	v_add_u32_e32 v7, v1, v5
	v_lshlrev_b32_e32 v9, 3, v6
	s_cselect_b32 s0, s1, s0
	v_ashrrev_i32_e32 v5, 6, v7
	v_and_b32_e32 v9, -16, v9
	s_add_i32 s0, s0, s39
	v_add_u32_e32 v9, v5, v9
	v_and_b32_e32 v10, 3, v5
	s_mul_hi_i32 s1, s0, 0x2e8ba2e9
	v_and_or_b32 v10, v9, s4, v10
	s_lshr_b32 s4, s1, 31
	s_ashr_i32 s1, s1, 4
	s_add_i32 s1, s1, s4
	s_lshl_b32 s4, s1, 2
	v_and_b32_e32 v7, 0xc0, v7
	s_sub_i32 s5, s3, s4
	v_sub_u32_e32 v1, v1, v7
	s_min_i32 s5, s5, 4
	v_ashrrev_i16_sdwa v1, v238, sext(v1) dst_sel:DWORD dst_unused:UNUSED_PAD src0_sel:DWORD src1_sel:BYTE_0
	s_abs_i32 s18, s5
	v_bfe_i32 v7, v1, 0, 16
	v_cvt_f32_u32_e32 v1, s18
	s_sub_i32 s20, 0, s18
	s_mul_i32 s1, s1, 88
	s_sub_i32 s0, s0, s1
	v_rcp_iflag_f32_e32 v1, v1
	s_abs_i32 s19, s0
	s_xor_b32 s1, s0, s5
	s_ashr_i32 s1, s1, 31
	v_mul_f32_e32 v1, 0x4f7ffffe, v1
	v_cvt_u32_f32_e32 v1, v1
	v_lshrrev_b32_e32 v11, 2, v9
	v_lshlrev_b32_e32 v12, 1, v9
	v_and_b32_e32 v11, 4, v11
	v_readfirstlane_b32 s21, v1
	s_mul_i32 s20, s20, s21
	s_mul_hi_u32 s20, s21, s20
	s_add_i32 s21, s21, s20
	s_mul_hi_u32 s20, s19, s21
	s_mul_i32 s21, s20, s18
	s_sub_i32 s19, s19, s21
	s_add_i32 s21, s20, 1
	s_sub_i32 s22, s19, s18
	s_cmp_ge_u32 s19, s18
	s_cselect_b32 s20, s21, s20
	s_cselect_b32 s19, s22, s19
	s_add_i32 s21, s20, 1
	s_cmp_ge_u32 s19, s18
	s_cselect_b32 s18, s21, s20
	s_xor_b32 s18, s18, s1
	s_sub_i32 s26, s18, s1
	s_mul_i32 s1, s26, s5
	s_sub_i32 s0, s0, s1
	s_add_i32 s28, s4, s0
	s_ashr_i32 s29, s28, 31
	s_lshl_b64 s[0:1], s[28:29], 19
	s_add_u32 s30, s14, s0
	s_addc_u32 s31, s15, s1
	s_ashr_i32 s27, s26, 31
	v_and_b32_e32 v12, 24, v12
	s_lshl_b64 s[0:1], s[26:27], 19
	v_or3_b32 v10, v10, v11, v12
	v_lshlrev_b32_e32 v11, 5, v6
	s_add_u32 s34, s41, s0
	v_and_b32_e32 v11, 32, v11
	s_addc_u32 s35, s42, s1
	s_add_i32 s4, s47, s7
	v_add_lshl_u32 v11, v11, v7, 1
	s_add_i32 s5, s4, 0x2000
	v_lshl_add_u32 v136, v10, 11, v11
	s_mov_b32 m0, s4
	s_add_u32 s0, s34, 0x40000
	global_load_lds_dwordx4 v136, s[34:35]
	s_mov_b32 m0, s5
	s_addc_u32 s1, s35, 0
	s_add_i32 s29, s50, s7
	global_load_lds_dwordx4 v132, s[34:35]
	s_mov_b32 m0, s29
	s_add_i32 s52, s29, 0x2000
	s_add_i32 s58, s2, s7
	global_load_lds_dwordx4 v136, s[0:1]
	s_mov_b32 m0, s52
	s_add_i32 s59, s58, 0x2000
	v_lshl_add_u32 v138, v9, 11, v11
	global_load_lds_dwordx4 v132, s[0:1]
	s_mov_b32 m0, s58
	s_add_u32 s0, s30, 0x40000
	global_load_lds_dwordx4 v138, s[30:31]
	s_mov_b32 m0, s59
	s_addc_u32 s1, s31, 0
	s_add_i32 s60, s58, 0x4000
	global_load_lds_dwordx4 v134, s[30:31]
	s_mov_b32 m0, s60
	s_add_i32 s61, s58, 0x6000
	global_load_lds_dwordx4 v138, s[0:1]
	s_mov_b32 m0, s61
	s_cmp_eq_u32 s13, 1
	global_load_lds_dwordx4 v134, s[0:1]
	s_cselect_b64 s[0:1], -1, 0
	s_cmp_lg_u32 s13, 1
	s_cbranch_scc1 .LBB13_1402
	s_barrier

;     __host__ __device__ bool next(int i, Unit& u) const {
;         const long L = (long)i * G + c; if (L >= nwg) return false;
;         int wgid = (int)L; { const int q = nwg / NXCD, r = nwg % NXCD, xcd = wgid % NXCD; int off = wgid / NXCD; if (rev & 2) off = (xcd < r ? q + 1 : q) - 1 - off;
;             wgid = (xcd < r ? xcd * (q + 1) : r * (q + 1) + (xcd - r) * q) + off; }
;         const int nig = wgm * nN, gid = wgid / nig, fm = gid * wgm, gsz = (nM - fm) < wgm ? (nM - fm) : wgm;
;         u.pm = fm + ((wgid % nig) % gsz); u.pn = (wgid % nig) / gsz; if (rev & 1) u.pn = nN - 1 - u.pn; return true;
.LBB13_1410:
	s_ashr_i32 s18, s20, 3
	s_add_i32 s18, s22, s18
	s_mul_hi_i32 s19, s18, 0x2e8ba2e9
	s_lshr_b32 s20, s19, 31
	s_ashr_i32 s19, s19, 4
	s_add_i32 s19, s19, s20
	s_lshl_b32 s20, s19, 2
	s_sub_i32 s21, s3, s20
	s_min_i32 s21, s21, 4
	s_abs_i32 s22, s21
	v_cvt_f32_u32_e32 v2, s22
	s_sub_i32 s24, 0, s22
	s_mul_i32 s19, s19, 88
	s_sub_i32 s19, s18, s19
	v_rcp_iflag_f32_e32 v2, v2
	s_abs_i32 s18, s19
	s_xor_b32 s23, s19, s21
	s_ashr_i32 s23, s23, 31
	v_mul_f32_e32 v2, 0x4f7ffffe, v2
	v_cvt_u32_f32_e32 v2, v2
	s_nop 0
	v_readfirstlane_b32 s25, v2
	s_mul_i32 s24, s24, s25
	s_mul_hi_u32 s24, s25, s24
	s_add_i32 s25, s25, s24
	s_mul_hi_u32 s24, s18, s25
	s_mul_i32 s25, s24, s22
	s_sub_i32 s18, s18, s25
	s_add_i32 s27, s24, 1
	s_sub_i32 s25, s18, s22
	s_cmp_ge_u32 s18, s22
	s_cselect_b32 s24, s27, s24
	s_cselect_b32 s18, s25, s18
	s_add_i32 s25, s24, 1
	s_cmp_ge_u32 s18, s22
	s_cselect_b32 s18, s25, s24
	s_xor_b32 s18, s18, s23
	s_sub_i32 s18, s18, s23
	s_mul_i32 s21, s18, s21
	s_sub_i32 s19, s19, s21
	s_add_i32 s20, s20, s19
